# m8 + scan helper STAGE: dropped 36 zero-initialisation moves in front of DPP moves (bound_ctrl instead)
# baseline (speedup 1.0000x reference)
.LBB0_796:
	s_andn2_b64 vcc, exec, s[14:15]
	s_mov_b32 s2, 64
	s_cbranch_vccnz .LBB0_805
	v_mov_b32_e32 v100, v124
	v_add_u32_e32 v108, s46, v167
	v_add_u32_e32 v100, s3, v167
	ds_read_b128 v[100:103], v100
	ds_read_b128 v[108:111], v108
	s_waitcnt vmcnt(9)
	v_lshlrev_b32_e32 v104, 16, v72
	v_and_b32_e32 v105, 0xffff0000, v72
	v_lshlrev_b32_e32 v106, 16, v73
	v_and_b32_e32 v107, 0xffff0000, v73
	s_waitcnt vmcnt(6)
	v_lshlrev_b32_e32 v49, 16, v80
	v_and_b32_e32 v122, 0xffff0000, v80
	v_lshlrev_b32_e32 v120, 16, v81
	v_and_b32_e32 v121, 0xffff0000, v81
	v_add_u32_e32 v146, s47, v167
	v_sub_f32_e32 v121, v121, v107
	v_sub_f32_e32 v120, v120, v106
	v_sub_f32_e32 v123, v122, v105
	v_sub_f32_e32 v122, v49, v104
	s_waitcnt lgkmcnt(1)
	v_pk_fma_f32 v[138:139], v[122:123], v[100:101], v[104:105]
	v_pk_fma_f32 v[140:141], v[120:121], v[102:103], v[106:107]
	v_add_u32_e32 v49, s48, v167
	ds_read_b128 v[104:107], v146
	ds_read_b128 v[100:103], v49
	v_lshlrev_b32_e32 v116, 16, v68
	v_and_b32_e32 v117, 0xffff0000, v68
	s_waitcnt vmcnt(5)
	v_lshlrev_b32_e32 v142, 16, v88
	v_and_b32_e32 v143, 0xffff0000, v88
	v_lshlrev_b32_e32 v118, 16, v69
	v_and_b32_e32 v119, 0xffff0000, v69
	v_lshlrev_b32_e32 v144, 16, v89
	v_and_b32_e32 v145, 0xffff0000, v89
	v_sub_f32_e32 v123, v143, v117
	v_sub_f32_e32 v122, v142, v116
	v_sub_f32_e32 v121, v145, v119
	v_sub_f32_e32 v120, v144, v118
	s_waitcnt lgkmcnt(2)
	v_pk_fma_f32 v[144:145], v[122:123], v[108:109], v[116:117]
	v_add_u32_e32 v49, s3, v168
	v_pk_fma_f32 v[146:147], v[120:121], v[110:111], v[118:119]
	s_waitcnt lgkmcnt(0)
	v_pk_mul_f32 v[142:143], v[144:145], v[100:101]
	v_add_u32_e32 v100, s46, v168
	ds_read_b128 v[108:111], v49
	ds_read_b128 v[116:119], v100
	v_add_u32_e32 v49, s47, v168
	v_add_u32_e32 v120, s48, v168
	v_pk_mul_f32 v[148:149], v[146:147], v[102:103]
	ds_read_b128 v[100:103], v49
	ds_read_b128 v[120:123], v120
	v_lshlrev_b32_e32 v130, 16, v70
	v_and_b32_e32 v131, 0xffff0000, v70
	v_lshlrev_b32_e32 v152, 16, v90
	v_and_b32_e32 v153, 0xffff0000, v90
	v_lshlrev_b32_e32 v134, 16, v71
	v_and_b32_e32 v135, 0xffff0000, v71
	v_lshlrev_b32_e32 v150, 16, v91
	v_and_b32_e32 v151, 0xffff0000, v91
	v_sub_f32_e32 v153, v153, v131
	v_sub_f32_e32 v152, v152, v130
	v_sub_f32_e32 v151, v151, v135
	v_sub_f32_e32 v150, v150, v134
	s_waitcnt lgkmcnt(2)
	v_pk_fma_f32 v[152:153], v[152:153], v[116:117], v[130:131]
	v_pk_fma_f32 v[150:151], v[150:151], v[118:119], v[134:135]
	s_waitcnt lgkmcnt(0)
	v_pk_mul_f32 v[156:157], v[152:153], v[120:121]
	v_pk_mul_f32 v[154:155], v[150:151], v[122:123]
	v_mov_b32_e32 v118, v143
	v_mov_b32_e32 v119, v157
	v_mov_b32_e32 v116, v142
	v_mov_b32_e32 v117, v156
	v_pk_mul_f32 v[118:119], v[118:119], v[118:119]
	v_mov_b32_e32 v120, v149
	v_mov_b32_e32 v121, v155
	v_pk_fma_f32 v[116:117], v[116:117], v[116:117], v[118:119]
	v_mov_b32_e32 v118, v148
	v_mov_b32_e32 v119, v154
	v_pk_mul_f32 v[120:121], v[120:121], v[120:121]
	s_mov_b32 s2, 0xf800000
	v_pk_fma_f32 v[118:119], v[118:119], v[118:119], v[120:121]
	v_lshlrev_b32_e32 v128, 16, v74
	v_pk_add_f32 v[116:117], v[116:117], v[118:119]
	v_and_b32_e32 v129, 0xffff0000, v74
	v_add_f32_e32 v49, v116, v117
	v_lshlrev_b32_e32 v158, 16, v82
	v_and_b32_e32 v159, 0xffff0000, v82
	v_add_f32_dpp v49, v49, v49 row_half_mirror row_mask:0xf bank_mask:0xf bound_ctrl:1
	v_sub_f32_e32 v119, v159, v129
	v_lshlrev_b32_e32 v132, 16, v75
	v_add_f32_dpp v49, v49, v49 quad_perm:[3,2,1,0] row_mask:0xf bank_mask:0xf bound_ctrl:1
	v_and_b32_e32 v133, 0xffff0000, v75
	v_lshlrev_b32_e32 v160, 16, v83
	v_add_f32_dpp v49, v49, v49 quad_perm:[1,0,3,2] row_mask:0xf bank_mask:0xf bound_ctrl:1
	v_mul_f32_e32 v116, 0x4f800000, v49
	v_cmp_gt_f32_e32 vcc, s2, v49
	v_and_b32_e32 v161, 0xffff0000, v83
	v_sub_f32_e32 v117, v161, v133
	v_cndmask_b32_e32 v49, v49, v116, vcc
	v_sqrt_f32_e32 v118, v49
	v_sub_f32_e32 v116, v160, v132
	s_waitcnt vmcnt(3)
	v_lshlrev_b32_e32 v50, 16, v92
	v_and_b32_e32 v51, 0xffff0000, v92
	v_add_u32_e32 v120, -1, v118
	v_fma_f32 v121, -v120, v118, v49
	v_cmp_ge_f32_e64 s[14:15], 0, v121
	v_add_u32_e32 v121, 1, v118
	v_lshlrev_b32_e32 v136, 16, v93
	v_cndmask_b32_e64 v120, v118, v120, s[14:15]
	v_fma_f32 v118, -v121, v118, v49
	v_cmp_lt_f32_e64 s[14:15], 0, v118
	v_and_b32_e32 v137, 0xffff0000, v93
	v_lshlrev_b32_e32 v112, 16, v94
	v_cndmask_b32_e64 v118, v120, v121, s[14:15]
	v_mul_f32_e32 v120, 0x37800000, v118
	v_cndmask_b32_e32 v118, v118, v120, vcc
	v_cmp_class_f32_e32 vcc, v49, v192
	v_and_b32_e32 v113, 0xffff0000, v94
	v_lshlrev_b32_e32 v114, 16, v95
	v_cndmask_b32_e32 v49, v118, v49, vcc
	v_max_f32_e32 v49, 0x2b8cbccc, v49
	v_div_scale_f32 v120, s[14:15], v49, v49, 1.0
	v_rcp_f32_e32 v121, v120
	v_sub_f32_e32 v118, v158, v128
	v_pk_fma_f32 v[130:131], v[118:119], v[108:109], v[128:129]
	v_pk_fma_f32 v[128:129], v[116:117], v[110:111], v[132:133]
	v_fma_f32 v108, -v120, v121, 1.0
	v_fmac_f32_e32 v121, v108, v121
	v_div_scale_f32 v108, vcc, 1.0, v49, 1.0
	v_mul_f32_e32 v109, v108, v121
	v_fma_f32 v110, -v120, v109, v108
	v_fmac_f32_e32 v109, v110, v121
	v_fma_f32 v108, -v120, v109, v108
	v_div_fmas_f32 v108, v108, v121, v109
	v_div_fixup_f32 v158, v108, v49, 1.0
	v_add_u32_e32 v49, s49, v167
	ds_read_b128 v[108:111], v49
	v_pk_add_f32 v[116:117], v[50:51], -1.0 op_sel_hi:[1,0]
	v_pk_add_f32 v[118:119], v[136:137], -1.0 op_sel_hi:[1,0]
	v_add_u32_e32 v49, s50, v167
	ds_read_b128 v[132:135], v49
	s_waitcnt lgkmcnt(1)
	v_pk_fma_f32 v[110:111], v[118:119], v[110:111], 1.0 op_sel_hi:[1,1,0]
	v_pk_fma_f32 v[108:109], v[116:117], v[108:109], 1.0 op_sel_hi:[1,1,0]
	v_add_u32_e32 v49, s49, v168
	v_pk_mul_f32 v[118:119], v[146:147], v[110:111]
	v_pk_mul_f32 v[116:117], v[144:145], v[108:109]
	ds_read_b128 v[108:111], v49
	v_pk_mul_f32 v[142:143], v[142:143], v[158:159] op_sel_hi:[1,0]
	v_and_b32_e32 v115, 0xffff0000, v95
	v_pk_mul_f32 v[194:195], v[148:149], v[158:159] op_sel_hi:[1,0]
	v_pk_mul_f32 v[120:121], v[142:143], v[50:51]
	v_pk_mul_f32 v[50:51], v[156:157], v[158:159] op_sel_hi:[1,0]
	v_pk_add_f32 v[144:145], v[112:113], -1.0 op_sel_hi:[1,0]
	v_pk_mul_f32 v[122:123], v[194:195], v[136:137]
	v_pk_mul_f32 v[136:137], v[154:155], v[158:159] op_sel_hi:[1,0]
	v_pk_add_f32 v[154:155], v[114:115], -1.0 op_sel_hi:[1,0]
	s_waitcnt lgkmcnt(0)
	v_pk_fma_f32 v[108:109], v[144:145], v[108:109], 1.0 op_sel_hi:[1,1,0]
	v_pk_mul_f32 v[112:113], v[50:51], v[112:113]
	v_pk_fma_f32 v[110:111], v[154:155], v[110:111], 1.0 op_sel_hi:[1,1,0]
	v_pk_mul_f32 v[108:109], v[152:153], v[108:109]
	v_pk_mul_f32 v[114:115], v[136:137], v[114:115]
	v_mov_b32_e32 v152, v131
	v_mov_b32_e32 v153, v139
	v_mov_b32_e32 v154, v113
	v_mov_b32_e32 v155, v121
	v_pk_mul_f32 v[110:111], v[150:151], v[110:111]
	v_mov_b32_e32 v144, v130
	v_mov_b32_e32 v145, v138
	v_mov_b32_e32 v150, v112
	v_mov_b32_e32 v151, v120
	v_pk_mul_f32 v[152:153], v[152:153], v[154:155]
	v_mov_b32_e32 v154, v129
	v_mov_b32_e32 v155, v141
	v_mov_b32_e32 v156, v115
	v_mov_b32_e32 v157, v123
	v_pk_mul_f32 v[162:163], v[138:139], v[116:117]
	v_add_u32_e32 v49, s50, v168
	v_pk_fma_f32 v[144:145], v[144:145], v[150:151], v[152:153]
	v_mov_b32_e32 v150, v128
	v_mov_b32_e32 v151, v140
	v_mov_b32_e32 v152, v114
	v_mov_b32_e32 v153, v122
	v_pk_mul_f32 v[154:155], v[154:155], v[156:157]
	ds_read_b128 v[146:149], v49
	v_pk_fma_f32 v[150:151], v[150:151], v[152:153], v[154:155]
	v_mov_b32_e32 v155, v132
	v_mov_b32_e32 v157, v162
	v_mov_b32_e32 v132, v139
	v_mov_b32_e32 v162, v117
	v_pk_mul_f32 v[160:161], v[140:141], v[118:119]
	v_mov_b32_e32 v154, v138
	v_mov_b32_e32 v156, v116
	v_pk_mul_f32 v[132:133], v[132:133], v[162:163]
	v_pk_mul_f32 v[152:153], v[130:131], v[108:109]
	v_pk_fma_f32 v[132:133], v[154:155], v[156:157], v[132:133]
	v_pk_mov_b32 v[154:155], v[140:141], v[134:135] op_sel:[1,0]
	v_pk_mov_b32 v[156:157], v[118:119], v[160:161] op_sel:[1,0]
	v_mov_b32_e32 v134, v140
	v_mov_b32_e32 v160, v118
	v_pk_mul_f32 v[134:135], v[134:135], v[160:161]
	v_pk_add_f32 v[144:145], v[144:145], v[150:151]
	v_pk_fma_f32 v[134:135], v[154:155], v[156:157], v[134:135]
	v_mov_b32_e32 v155, v152
	v_pk_add_f32 v[132:133], v[132:133], v[134:135]
	s_waitcnt lgkmcnt(0)
	v_mov_b32_e32 v135, v146
	v_mov_b32_e32 v146, v131
	v_mov_b32_e32 v152, v109
	v_add_f32_e32 v49, 0, v145
	v_pk_mul_f32 v[150:151], v[128:129], v[110:111]
	v_mov_b32_e32 v134, v130
	v_mov_b32_e32 v154, v108
	v_pk_mul_f32 v[146:147], v[146:147], v[152:153]
	v_add_f32_e32 v49, v144, v49
	v_pk_fma_f32 v[134:135], v[134:135], v[154:155], v[146:147]
	v_pk_mov_b32 v[146:147], v[128:129], v[148:149] op_sel:[1,0]
	v_pk_mov_b32 v[152:153], v[110:111], v[150:151] op_sel:[1,0]
	v_mov_b32_e32 v148, v128
	v_mov_b32_e32 v150, v110
	s_and_b32 s44, s52, 1
	v_add_f32_dpp v49, v49, v49 row_half_mirror row_mask:0xf bank_mask:0xf bound_ctrl:1
	v_pk_mul_f32 v[148:149], v[148:149], v[150:151]
	s_lshl_b32 s2, s44, 13
	v_add_f32_dpp v49, v49, v49 quad_perm:[3,2,1,0] row_mask:0xf bank_mask:0xf bound_ctrl:1
	v_pk_fma_f32 v[146:147], v[146:147], v[152:153], v[148:149]
	v_pk_add_f32 v[132:133], v[132:133], 0 op_sel_hi:[1,0]
	v_add_f32_dpp v144, v49, v49 quad_perm:[1,0,3,2] row_mask:0xf bank_mask:0xf bound_ctrl:1
	v_pk_add_f32 v[134:135], v[134:135], v[146:147]
	v_add_u32_e32 v145, s2, v172
	v_mov_b32_e32 v164, v48
	v_mov_b32_e32 v165, v48
	v_pk_add_f32 v[132:133], v[132:133], v[134:135]
	v_mov_b32_e32 v134, v48
	v_mov_b32_e32 v135, v48
	v_pk_mul_f32 v[156:157], v[142:143], v[144:145] op_sel_hi:[1,0]
	v_pk_mul_f32 v[154:155], v[194:195], v[144:145] op_sel_hi:[1,0]
	s_waitcnt vmcnt(0)
	v_mov_b32_dpp v162, v8 row_shr:8 row_mask:0xf bank_mask:0xf bound_ctrl:1
	v_mov_b32_dpp v163, v9 row_shr:8 row_mask:0xf bank_mask:0xf bound_ctrl:1
	v_mov_b32_dpp v164, v10 row_shr:8 row_mask:0xf bank_mask:0xf
	v_mov_b32_dpp v165, v11 row_shr:8 row_mask:0xf bank_mask:0xf
	v_mov_b32_dpp v134, v132 row_half_mirror row_mask:0xf bank_mask:0xf
	v_mov_b32_dpp v135, v133 row_half_mirror row_mask:0xf bank_mask:0xf
	v_xor_b32_e32 v160, 0x80000000, v142
	v_xor_b32_e32 v161, 0x80000000, v143
	v_xor_b32_e32 v158, 0x80000000, v194
	v_xor_b32_e32 v159, 0x80000000, v195
	v_pk_fma_f32 v[154:155], v[10:11], v[140:141], v[154:155] neg_lo:[0,0,1] neg_hi:[0,0,1]
	v_pk_fma_f32 v[156:157], v[8:9], v[138:139], v[156:157] neg_lo:[0,0,1] neg_hi:[0,0,1]
	v_pk_mul_f32 v[138:139], v[142:143], v[162:163] neg_lo:[1,0] neg_hi:[1,0]
	v_pk_mul_f32 v[140:141], v[194:195], v[164:165] neg_lo:[1,0] neg_hi:[1,0]
	v_pk_add_f32 v[132:133], v[132:133], v[134:135]
	v_mov_b32_e32 v134, v48
	v_mov_b32_e32 v135, v48
	v_cndmask_b32_e64 v194, v141, v159, s[0:1]
	v_cndmask_b32_e64 v195, v140, v158, s[0:1]
	v_cndmask_b32_e64 v197, v139, v161, s[0:1]
	v_cndmask_b32_e64 v198, v138, v160, s[0:1]
	v_pk_mul_f32 v[138:139], v[156:157], v[162:163]
	v_pk_mul_f32 v[140:141], v[154:155], v[164:165]
	v_mov_b32_dpp v134, v132 quad_perm:[3,2,1,0] row_mask:0xf bank_mask:0xf
	v_mov_b32_dpp v135, v133 quad_perm:[3,2,1,0] row_mask:0xf bank_mask:0xf
	v_add_u32_e32 v193, s2, v171
	v_cndmask_b32_e64 v141, v141, v155, s[0:1]
	v_cndmask_b32_e64 v199, v140, v154, s[0:1]
	v_cndmask_b32_e64 v140, v139, v157, s[0:1]
	v_cndmask_b32_e64 v200, v138, v156, s[0:1]
	v_mov_b32_e32 v49, v48
	v_pk_add_f32 v[132:133], v[132:133], v[134:135]
	v_lshl_add_u32 v196, s44, 14, v173
	v_cvt_pk_bf16_f32 v138, v198, v197
	v_cvt_pk_bf16_f32 v139, v195, v194
	v_cvt_pk_bf16_f32 v140, v200, v140
	v_cvt_pk_bf16_f32 v141, v199, v141
	v_add_u32_e32 v194, v193, v183
	v_mov_b32_dpp v134, v132 quad_perm:[1,0,3,2] row_mask:0xf bank_mask:0xf bound_ctrl:1
	v_mov_b32_dpp v135, v133 quad_perm:[1,0,3,2] row_mask:0xf bank_mask:0xf bound_ctrl:1
	v_mov_b32_dpp v146, v120 row_shr:8 row_mask:0xf bank_mask:0xf bound_ctrl:1
	v_mov_b32_dpp v149, v116 row_shr:8 row_mask:0xf bank_mask:0xf bound_ctrl:1
	v_mov_b32_dpp v148, v121 row_shr:8 row_mask:0xf bank_mask:0xf bound_ctrl:1
	v_mov_b32_dpp v147, v117 row_shr:8 row_mask:0xf bank_mask:0xf bound_ctrl:1
	v_mov_b32_dpp v150, v122 row_shr:8 row_mask:0xf bank_mask:0xf bound_ctrl:1
	v_mov_b32_dpp v153, v118 row_shr:8 row_mask:0xf bank_mask:0xf bound_ctrl:1
	v_mov_b32_dpp v152, v123 row_shr:8 row_mask:0xf bank_mask:0xf bound_ctrl:1
	v_mov_b32_dpp v151, v119 row_shr:8 row_mask:0xf bank_mask:0xf bound_ctrl:1
	ds_write2_b64 v194, v[138:139], v[140:141] offset1:16
	v_add_u32_e32 v195, v145, v167
	v_add_u32_e32 v194, v196, v167
	v_mov_b64_e32 v[140:141], v[48:49]
	v_mov_b64_e32 v[138:139], v[48:49]
	s_and_saveexec_b64 s[14:15], s[4:5]
	s_cbranch_execz .LBB0_799
	v_pk_mul_f32 v[140:141], v[10:11], v[164:165]
	v_pk_mul_f32 v[138:139], v[8:9], v[162:163]
	ds_write_b128 v195, v[138:141] offset:16384
	v_mov_b32_e32 v138, v150
	v_mov_b32_e32 v139, v152
	v_pk_mul_f32 v[140:141], v[10:11], v[138:139]
	v_mov_b32_e32 v138, v146
	v_mov_b32_e32 v139, v148
	v_pk_mul_f32 v[138:139], v[8:9], v[138:139]
	ds_write_b128 v194, v[138:141] offset:32768
	v_mov_b32_e32 v138, v153
	v_mov_b32_e32 v139, v151
	v_pk_mul_f32 v[140:141], v[10:11], v[138:139]
	v_mov_b32_e32 v138, v149
	v_mov_b32_e32 v139, v147
	v_pk_mul_f32 v[138:139], v[8:9], v[138:139]
	ds_write_b128 v194, v[138:141] offset:33024
	ds_write_b128 v194, v[120:123] offset:33280
	ds_write_b128 v194, v[116:119] offset:33536
	v_pk_mul_f32 v[116:117], v[142:143], v[146:147] neg_lo:[1,0] neg_hi:[1,0]
	v_pk_mul_f32 v[118:119], v[158:159], v[150:151]
	v_pk_fma_f32 v[116:117], v[160:161], v[148:149], v[116:117] op_sel:[1,0,0] op_sel_hi:[0,1,1]
	v_pk_fma_f32 v[118:119], v[158:159], v[152:153], v[118:119] op_sel:[1,0,0] op_sel_hi:[0,1,1]
	v_pk_add_f32 v[116:117], v[116:117], v[118:119]
	v_pk_mul_f32 v[118:119], v[154:155], v[150:151]
	v_pk_add_f32 v[140:141], v[116:117], 0 op_sel_hi:[1,0]
	v_pk_mul_f32 v[116:117], v[156:157], v[146:147]
	v_pk_fma_f32 v[118:119], v[154:155], v[152:153], v[118:119] op_sel:[1,0,0] op_sel_hi:[0,1,1]
	v_pk_fma_f32 v[116:117], v[156:157], v[148:149], v[116:117] op_sel:[1,0,0] op_sel_hi:[0,1,1]
	v_pk_add_f32 v[116:117], v[116:117], v[118:119]
	s_nop 0
	v_pk_add_f32 v[138:139], v[116:117], 0 op_sel_hi:[1,0]
.LBB0_799:
	s_or_b64 exec, exec, s[14:15]
	s_mul_hi_u32 s2, s52, 0xaaaaaaab
	s_lshr_b32 s2, s2, 1
	s_mul_i32 s2, s2, 3
	v_lshlrev_b32_e32 v120, 16, v76
	v_and_b32_e32 v121, 0xffff0000, v76
	v_lshlrev_b32_e32 v122, 16, v77
	v_and_b32_e32 v123, 0xffff0000, v77
	v_lshlrev_b32_e32 v49, 16, v84
	v_and_b32_e32 v142, 0xffff0000, v84
	v_lshlrev_b32_e32 v146, 16, v85
	v_and_b32_e32 v147, 0xffff0000, v85
	s_sub_i32 s2, s52, s2
	v_sub_f32_e32 v143, v142, v121
	v_sub_f32_e32 v142, v49, v120
	v_sub_f32_e32 v147, v147, v123
	v_sub_f32_e32 v146, v146, v122
	s_lshl_b32 s14, s2, 13
	v_mov_b32_e32 v145, v144
	v_pk_fma_f32 v[106:107], v[146:147], v[106:107], v[122:123]
	v_pk_fma_f32 v[104:105], v[142:143], v[104:105], v[120:121]
	v_add_u32_e32 v49, s14, v177
	ds_write_b128 v49, v[104:107]
	v_mov_b32_e32 v104, v144
	v_mov_b32_e32 v105, v144
	v_pk_mul_f32 v[120:121], v[50:51], v[144:145]
	v_pk_mul_f32 v[122:123], v[136:137], v[104:105]
	v_mov_b32_dpp v144, v12 row_shr:8 row_mask:0xf bank_mask:0xf bound_ctrl:1
	v_mov_b32_dpp v145, v13 row_shr:8 row_mask:0xf bank_mask:0xf bound_ctrl:1
	v_mov_b32_dpp v146, v14 row_shr:8 row_mask:0xf bank_mask:0xf bound_ctrl:1
	v_mov_b32_dpp v147, v15 row_shr:8 row_mask:0xf bank_mask:0xf bound_ctrl:1
	v_xor_b32_e32 v137, 0x80000000, v137
	v_xor_b32_e32 v136, 0x80000000, v136
	v_xor_b32_e32 v142, 0x80000000, v50
	v_xor_b32_e32 v143, 0x80000000, v51
	v_pk_fma_f32 v[120:121], v[12:13], v[130:131], v[120:121] neg_lo:[0,0,1] neg_hi:[0,0,1]
	v_pk_fma_f32 v[122:123], v[14:15], v[128:129], v[122:123] neg_lo:[0,0,1] neg_hi:[0,0,1]
	v_pk_mul_f32 v[128:129], v[136:137], v[146:147]
	v_pk_mul_f32 v[130:131], v[50:51], v[144:145] neg_lo:[1,0] neg_hi:[1,0]
	v_lshlrev_b32_e32 v116, 16, v96
	v_and_b32_e32 v117, 0xffff0000, v96
	v_lshlrev_b32_e32 v118, 16, v97
	v_and_b32_e32 v119, 0xffff0000, v97
	v_add_u32_e32 v148, s14, v169
	v_cndmask_b32_e64 v149, v129, v137, s[0:1]
	v_cndmask_b32_e64 v150, v128, v136, s[0:1]
	v_cndmask_b32_e64 v151, v131, v143, s[0:1]
	v_cndmask_b32_e64 v152, v130, v142, s[0:1]
	v_pk_mul_f32 v[128:129], v[120:121], v[144:145]
	v_pk_mul_f32 v[130:131], v[122:123], v[146:147]
	ds_write_b128 v148, v[116:119]
	v_cndmask_b32_e64 v131, v131, v123, s[0:1]
	v_cndmask_b32_e64 v153, v130, v122, s[0:1]
	v_cndmask_b32_e64 v130, v129, v121, s[0:1]
	v_cndmask_b32_e64 v154, v128, v120, s[0:1]
	v_mov_b32_dpp v104, v112 row_shr:8 row_mask:0xf bank_mask:0xf bound_ctrl:1
	v_mov_b32_dpp v107, v108 row_shr:8 row_mask:0xf bank_mask:0xf bound_ctrl:1
	v_mov_b32_dpp v106, v113 row_shr:8 row_mask:0xf bank_mask:0xf bound_ctrl:1
	v_mov_b32_dpp v105, v109 row_shr:8 row_mask:0xf bank_mask:0xf bound_ctrl:1
	v_mov_b32_dpp v116, v114 row_shr:8 row_mask:0xf bank_mask:0xf bound_ctrl:1
	v_mov_b32_dpp v119, v110 row_shr:8 row_mask:0xf bank_mask:0xf bound_ctrl:1
	v_mov_b32_dpp v118, v115 row_shr:8 row_mask:0xf bank_mask:0xf bound_ctrl:1
	v_mov_b32_dpp v117, v111 row_shr:8 row_mask:0xf bank_mask:0xf bound_ctrl:1
	v_cvt_pk_bf16_f32 v128, v152, v151
	v_cvt_pk_bf16_f32 v129, v150, v149
	v_cvt_pk_bf16_f32 v130, v154, v130
	v_cvt_pk_bf16_f32 v131, v153, v131
	v_add_u32_e32 v149, v193, v184
	ds_write2_b64 v149, v[128:129], v[130:131] offset1:16
	s_and_saveexec_b64 s[14:15], s[4:5]
	s_cbranch_execz .LBB0_801
	v_pk_mul_f32 v[130:131], v[14:15], v[146:147]
	v_pk_mul_f32 v[128:129], v[12:13], v[144:145]
	ds_write_b128 v195, v[128:131] offset:16400
	v_mov_b32_e32 v128, v116
	v_mov_b32_e32 v129, v118
	v_pk_mul_f32 v[130:131], v[14:15], v[128:129]
	v_mov_b32_e32 v128, v104
	v_mov_b32_e32 v129, v106
	v_pk_mul_f32 v[128:129], v[12:13], v[128:129]
	ds_write_b128 v194, v[128:131] offset:32784
	v_mov_b32_e32 v128, v119
	v_mov_b32_e32 v129, v117
	v_pk_mul_f32 v[130:131], v[14:15], v[128:129]
	v_mov_b32_e32 v128, v107
	v_mov_b32_e32 v129, v105
	v_pk_mul_f32 v[128:129], v[12:13], v[128:129]
	ds_write_b128 v194, v[128:131] offset:33040
	ds_write_b128 v194, v[112:115] offset:33296
	ds_write_b128 v194, v[108:111] offset:33552
	v_pk_mul_f32 v[50:51], v[50:51], v[104:105] neg_lo:[1,0] neg_hi:[1,0]
	v_pk_mul_f32 v[108:109], v[136:137], v[116:117]
	v_pk_fma_f32 v[50:51], v[142:143], v[106:107], v[50:51] op_sel:[1,0,0] op_sel_hi:[0,1,1]
	v_pk_fma_f32 v[108:109], v[136:137], v[118:119], v[108:109] op_sel:[1,0,0] op_sel_hi:[0,1,1]
	v_pk_add_f32 v[50:51], v[50:51], v[108:109]
	s_nop 0
	v_pk_add_f32 v[140:141], v[140:141], v[50:51]
	v_pk_mul_f32 v[50:51], v[120:121], v[104:105]
	v_pk_mul_f32 v[104:105], v[122:123], v[116:117]
	v_pk_fma_f32 v[50:51], v[120:121], v[106:107], v[50:51] op_sel:[1,0,0] op_sel_hi:[0,1,1]
	v_pk_fma_f32 v[104:105], v[122:123], v[118:119], v[104:105] op_sel:[1,0,0] op_sel_hi:[0,1,1]
	v_pk_add_f32 v[50:51], v[50:51], v[104:105]
	s_nop 0
	v_pk_add_f32 v[138:139], v[138:139], v[50:51]
.LBB0_801:
	s_or_b64 exec, exec, s[14:15]
	v_lshlrev_b32_e32 v50, 16, v78
	v_and_b32_e32 v51, 0xffff0000, v78
	v_lshlrev_b32_e32 v108, 16, v79
	v_and_b32_e32 v109, 0xffff0000, v79
	v_lshlrev_b32_e32 v110, 16, v86
	v_and_b32_e32 v111, 0xffff0000, v86
	v_lshlrev_b32_e32 v112, 16, v87
	v_and_b32_e32 v113, 0xffff0000, v87
	v_sub_f32_e32 v111, v111, v51
	v_sub_f32_e32 v110, v110, v50
	v_sub_f32_e32 v113, v113, v109
	v_sub_f32_e32 v112, v112, v108
	v_pk_fma_f32 v[102:103], v[112:113], v[102:103], v[108:109]
	v_pk_fma_f32 v[100:101], v[110:111], v[100:101], v[50:51]
	v_lshlrev_b32_e32 v104, 16, v98
	v_and_b32_e32 v105, 0xffff0000, v98
	v_lshlrev_b32_e32 v106, 16, v99
	v_and_b32_e32 v107, 0xffff0000, v99
	ds_write_b128 v49, v[100:103] offset:16
	ds_write_b128 v148, v[104:107] offset:16
	v_mov_b32_dpp v50, v140 row_half_mirror row_mask:0xf bank_mask:0xf bound_ctrl:1
	v_mov_b32_dpp v51, v141 row_half_mirror row_mask:0xf bank_mask:0xf bound_ctrl:1
	v_mov_b32_dpp v102, v138 row_half_mirror row_mask:0xf bank_mask:0xf bound_ctrl:1
	v_mov_b32_dpp v103, v139 row_half_mirror row_mask:0xf bank_mask:0xf bound_ctrl:1
	v_pk_add_f32 v[50:51], v[140:141], v[50:51]
	v_pk_add_f32 v[102:103], v[138:139], v[102:103]
	s_nop 0
	v_mov_b32_dpp v100, v50 quad_perm:[3,2,1,0] row_mask:0xf bank_mask:0xf bound_ctrl:1
	v_mov_b32_dpp v101, v51 quad_perm:[3,2,1,0] row_mask:0xf bank_mask:0xf bound_ctrl:1
	v_mov_b32_dpp v104, v102 quad_perm:[3,2,1,0] row_mask:0xf bank_mask:0xf bound_ctrl:1
	v_mov_b32_dpp v105, v103 quad_perm:[3,2,1,0] row_mask:0xf bank_mask:0xf bound_ctrl:1
	v_pk_add_f32 v[50:51], v[50:51], v[100:101]
	v_pk_add_f32 v[102:103], v[102:103], v[104:105]
	s_nop 0
	v_mov_b32_dpp v100, v50 quad_perm:[1,0,3,2] row_mask:0xf bank_mask:0xf bound_ctrl:1
	v_mov_b32_dpp v101, v51 quad_perm:[1,0,3,2] row_mask:0xf bank_mask:0xf bound_ctrl:1
	v_mov_b32_dpp v104, v102 quad_perm:[1,0,3,2] row_mask:0xf bank_mask:0xf bound_ctrl:1
	v_mov_b32_dpp v105, v103 quad_perm:[1,0,3,2] row_mask:0xf bank_mask:0xf bound_ctrl:1
	s_and_saveexec_b64 s[14:15], s[6:7]
	s_cbranch_execz .LBB0_804
	v_pk_add_f32 v[106:107], v[132:133], v[134:135]
	v_lshl_add_u32 v49, s2, 8, v170
	ds_write_b64 v49, v[106:107]
	s_and_b64 exec, exec, s[4:5]
	v_lshl_add_u32 v49, s44, 8, v174
	v_pk_add_f32 v[102:103], v[102:103], v[104:105]
	v_pk_add_f32 v[100:101], v[50:51], v[100:101]
	ds_write_b128 v49, v[100:103]
